# short-conv part of MIX: loop-head vmcnt(0), which only drained the previous item's four stores, removed
# speedup vs baseline: 1.0019x; 1.0019x over previous
.LBB0_203:
	s_mov_b32 s4, 0x2aaaaaab
	v_mul_hi_i32 v2, v72, s4
	v_lshrrev_b32_e32 v3, 31, v2
	v_ashrrev_i32_e32 v2, 4, v2
	v_add_u32_e32 v4, v2, v3
	s_movk_i32 s4, 0xfd00
	v_lshlrev_b32_e32 v73, 2, v4
	v_mad_u64_u32 v[6:7], s[4:5], v4, s4, v[0:1]
	v_mov_b64_e32 v[2:3], s[28:29]
	v_mad_i64_i32 v[2:3], s[4:5], v73, s93, v[2:3]
	v_ashrrev_i32_e32 v7, 31, v6
	v_and_b32_e32 v4, 0x3ff, v4
	v_mov_b32_e32 v50, 0
	v_cmp_ne_u32_e64 s[6:7], 0, v4
	v_lshl_add_u64 v[4:5], v[6:7], 1, v[2:3]
	v_mov_b32_e32 v58, 0
	v_mov_b32_e32 v59, 0
	v_mov_b32_e32 v60, 0
	v_mov_b32_e32 v61, 0
	v_mov_b32_e32 v62, 0
	v_mov_b32_e32 v63, 0
	v_mov_b32_e32 v64, 0
	v_mov_b32_e32 v65, 0
	s_and_saveexec_b64 s[4:5], s[6:7]
	s_cbranch_execz .LBB0_205
	v_add_co_u32_e32 v8, vcc, 0xffff5000, v4
	s_nop 1
	v_addc_co_u32_e32 v9, vcc, -1, v5, vcc
	global_load_dwordx4 v[58:61], v[8:9], off offset:-3072 nt
	global_load_dwordx4 v[62:65], v[8:9], off nt
